# GDN section e: waves 1-7 pre-read their TB-independent operands (VBT / KBGT fragments) at the end of section d; section e rewritten with batched reads and back-to-back MFMA chains
# speedup vs baseline: 1.0081x; 1.0010x over previous
.Lgp_cn4:
.Lgp_pre:
	v_and_b32_e32 v0, 15, v215
	v_lshrrev_b32_e32 v1, 4, v215
	v_bfe_u32 v5, v215, 1, 3
	v_xor_b32_e32 v2, v1, v5
	v_add_u32_e32 v6, 4, v1
	v_xor_b32_e32 v3, v6, v5
	v_lshlrev_b32_e32 v2, 4, v2
	v_lshlrev_b32_e32 v3, 4, v3
	s_cmp_lt_u32 s82, 4
	s_cbranch_scc1 .Lgp_pre_u
	v_readlane_b32 s20, v253, 53
	s_nop 3
	v_mul_u32_u24_e32 v5, 0x90, v0
	s_mul_i32 s21, s20, 0x90
	s_add_i32 s21, s21, 0x11400
	v_add_u32_e32 v8, s21, v5
	v_add_u32_e32 v9, 0x900, v8
	v_add_u32_e32 v6, v8, v2
	ds_read_b128 v[48:51], v6
	v_add_u32_e32 v6, v8, v3
	ds_read_b128 v[52:55], v6
	v_add_u32_e32 v6, v9, v2
	ds_read_b128 v[56:59], v6
	v_add_u32_e32 v6, v9, v3
	ds_read_b128 v[60:63], v6
	s_branch .LBB0_337
.Lgp_pre_u:
	v_mul_u32_u24_e32 v5, 0x90, v0
	v_add_u32_e32 v9, 0xcc00, v5
	v_add_u32_e32 v10, v9, v3
	v_add_u32_e32 v9, v9, v2
	ds_read_b128 v[56:59], v9
	ds_read_b128 v[60:63], v10
	ds_read_b128 v[64:67], v9 offset:2304
	ds_read_b128 v[68:71], v10 offset:2304
	ds_read_b128 v[72:75], v9 offset:4608
	ds_read_b128 v[76:79], v10 offset:4608
	ds_read_b128 v[80:83], v9 offset:6912
	ds_read_b128 v[84:87], v10 offset:6912
	ds_read_b128 v[88:91], v9 offset:9216
	ds_read_b128 v[92:95], v10 offset:9216
	ds_read_b128 v[96:99], v9 offset:11520
	ds_read_b128 v[100:103], v10 offset:11520
	ds_read_b128 v[104:107], v9 offset:13824
	ds_read_b128 v[108:111], v10 offset:13824
	ds_read_b128 v[112:115], v9 offset:16128
	ds_read_b128 v[116:119], v10 offset:16128

.LBB0_342:
	s_waitcnt lgkmcnt(0)
	s_barrier
	v_and_b32_e32 v0, 15, v215
	v_lshrrev_b32_e32 v1, 4, v215
	v_bfe_u32 v5, v215, 1, 3
	v_xor_b32_e32 v2, v1, v5
	v_add_u32_e32 v6, 4, v1
	v_xor_b32_e32 v3, v6, v5
	v_lshlrev_b32_e32 v2, 4, v2
	v_lshlrev_b32_e32 v3, 4, v3
	s_and_b64 vcc, exec, s[2:3]
	s_cbranch_vccnz .Lge_u
	v_readlane_b32 s0, v253, 53
	v_mul_u32_u24_e32 v5, 0x90, v0
	v_lshl_add_u32 v10, v1, 4, v5
	v_add_u32_e32 v10, 0x1a000, v10
	ds_read_b128 v[64:67], v10
	ds_read_b128 v[68:71], v10 offset:64
	ds_read_b128 v[72:75], v10 offset:2304
	ds_read_b128 v[76:79], v10 offset:2368
	ds_read_b128 v[80:83], v10 offset:4608
	ds_read_b128 v[84:87], v10 offset:4672
	ds_read_b128 v[88:91], v10 offset:6912
	ds_read_b128 v[92:95], v10 offset:6976
	s_lshl_b32 s20, s0, 6
	v_lshlrev_b32_e32 v4, 4, v0
	v_and_b32_e32 v5, 1, v1
	v_lshl_add_u32 v4, v5, 9, v4
	v_lshrrev_b32_e32 v5, 1, v1
	v_lshl_add_u32 v4, v5, 3, v4
	v_add_u32_e32 v4, s20, v4
	v_add_u32_e32 v5, 0x2000, v4
	s_waitcnt lgkmcnt(6)
	v_mfma_f32_16x16x32_bf16 v[16:19], v[48:51], v[64:67], 0
	v_mfma_f32_16x16x32_bf16 v[16:19], v[52:55], v[68:71], v[16:19]
	v_mfma_f32_16x16x32_bf16 v[32:35], v[56:59], v[64:67], 0
	v_mfma_f32_16x16x32_bf16 v[32:35], v[60:63], v[68:71], v[32:35]
	s_waitcnt lgkmcnt(4)
	v_mfma_f32_16x16x32_bf16 v[20:23], v[48:51], v[72:75], 0
	v_mfma_f32_16x16x32_bf16 v[20:23], v[52:55], v[76:79], v[20:23]
	v_mfma_f32_16x16x32_bf16 v[36:39], v[56:59], v[72:75], 0
	v_mfma_f32_16x16x32_bf16 v[36:39], v[60:63], v[76:79], v[36:39]
	s_waitcnt lgkmcnt(2)
	v_mfma_f32_16x16x32_bf16 v[24:27], v[48:51], v[80:83], 0
	v_mfma_f32_16x16x32_bf16 v[24:27], v[52:55], v[84:87], v[24:27]
	v_mfma_f32_16x16x32_bf16 v[40:43], v[56:59], v[80:83], 0
	v_mfma_f32_16x16x32_bf16 v[40:43], v[60:63], v[84:87], v[40:43]
	s_waitcnt lgkmcnt(0)
	v_mfma_f32_16x16x32_bf16 v[28:31], v[48:51], v[88:91], 0
	v_mfma_f32_16x16x32_bf16 v[28:31], v[52:55], v[92:95], v[28:31]
	v_mfma_f32_16x16x32_bf16 v[44:47], v[56:59], v[88:91], 0
	v_mfma_f32_16x16x32_bf16 v[44:47], v[60:63], v[92:95], v[44:47]
	s_nop 7
	v_cvt_pk_bf16_f32 v16, v16, v17
	v_cvt_pk_bf16_f32 v17, v18, v19
	global_store_dwordx2 v4, v[16:17], s[78:79]
	v_cvt_pk_bf16_f32 v20, v20, v21
	v_cvt_pk_bf16_f32 v21, v22, v23
	global_store_dwordx2 v4, v[20:21], s[78:79] offset:256
	v_cvt_pk_bf16_f32 v24, v24, v25
	v_cvt_pk_bf16_f32 v25, v26, v27
	global_store_dwordx2 v5, v[24:25], s[78:79]
	v_cvt_pk_bf16_f32 v28, v28, v29
	v_cvt_pk_bf16_f32 v29, v30, v31
	global_store_dwordx2 v5, v[28:29], s[78:79] offset:256
	v_cvt_pk_bf16_f32 v32, v32, v33
	v_cvt_pk_bf16_f32 v33, v34, v35
	global_store_dwordx2 v4, v[32:33], s[78:79] offset:1024
	v_cvt_pk_bf16_f32 v36, v36, v37
	v_cvt_pk_bf16_f32 v37, v38, v39
	global_store_dwordx2 v4, v[36:37], s[78:79] offset:1280
	v_cvt_pk_bf16_f32 v40, v40, v41
	v_cvt_pk_bf16_f32 v41, v42, v43
	global_store_dwordx2 v5, v[40:41], s[78:79] offset:1024
	v_cvt_pk_bf16_f32 v44, v44, v45
	v_cvt_pk_bf16_f32 v45, v46, v47
	global_store_dwordx2 v5, v[44:45], s[78:79] offset:1280
	s_branch .LBB0_220
.Lge_u:
	v_mul_u32_u24_e32 v5, 0x90, v0
	s_mul_i32 s20, s10, 0x90
	s_add_i32 s20, s20, 0x1a000
	v_lshl_add_u32 v8, v1, 4, v5
	v_add_u32_e32 v8, s20, v8
	ds_read_b128 v[48:51], v8
	ds_read_b128 v[52:55], v8 offset:64
	s_cmp_lg_u32 s10, 0
	s_cbranch_scc1 .Lge_u_st
	v_mul_u32_u24_e32 v5, 0x90, v0
	v_add_u32_e32 v9, 0xcc00, v5
	v_add_u32_e32 v10, v9, v3
	v_add_u32_e32 v9, v9, v2
	ds_read_b128 v[56:59], v9
	ds_read_b128 v[60:63], v10
	ds_read_b128 v[64:67], v9 offset:2304
	ds_read_b128 v[68:71], v10 offset:2304
	ds_read_b128 v[72:75], v9 offset:4608
	ds_read_b128 v[76:79], v10 offset:4608
	ds_read_b128 v[80:83], v9 offset:6912
	ds_read_b128 v[84:87], v10 offset:6912
	ds_read_b128 v[88:91], v9 offset:9216
	ds_read_b128 v[92:95], v10 offset:9216
	ds_read_b128 v[96:99], v9 offset:11520
	ds_read_b128 v[100:103], v10 offset:11520
	ds_read_b128 v[104:107], v9 offset:13824
	ds_read_b128 v[108:111], v10 offset:13824
	ds_read_b128 v[112:115], v9 offset:16128
	ds_read_b128 v[116:119], v10 offset:16128
.Lge_u_st:
	s_add_u32 s0, s78, 0xe000
	s_addc_u32 s1, s79, 0
	s_lshr_b32 s20, s10, 5
	s_lshl_b32 s20, s20, 11
	s_and_b32 s21, s10, 16
	s_add_i32 s20, s20, s21
	v_lshlrev_b32_e32 v4, 5, v0
	v_and_b32_e32 v5, 1, v1
	v_lshl_add_u32 v4, v5, 10, v4
	v_lshrrev_b32_e32 v5, 1, v1
	v_lshl_add_u32 v4, v5, 3, v4
	v_add_u32_e32 v4, s20, v4
	v_add_u32_e32 v5, 0x1000, v4
	v_add_u32_e32 v6, 0x2000, v4
	v_add_u32_e32 v11, 0x3000, v4
	s_waitcnt lgkmcnt(0)
	v_mfma_f32_16x16x32_bf16 v[16:19], v[48:51], v[56:59], 0
	v_mfma_f32_16x16x32_bf16 v[16:19], v[52:55], v[60:63], v[16:19]
	v_mfma_f32_16x16x32_bf16 v[20:23], v[48:51], v[64:67], 0
	v_mfma_f32_16x16x32_bf16 v[20:23], v[52:55], v[68:71], v[20:23]
	v_mfma_f32_16x16x32_bf16 v[24:27], v[48:51], v[72:75], 0
	v_mfma_f32_16x16x32_bf16 v[24:27], v[52:55], v[76:79], v[24:27]
	v_mfma_f32_16x16x32_bf16 v[28:31], v[48:51], v[80:83], 0
	v_mfma_f32_16x16x32_bf16 v[28:31], v[52:55], v[84:87], v[28:31]
	v_mfma_f32_16x16x32_bf16 v[32:35], v[48:51], v[88:91], 0
	v_mfma_f32_16x16x32_bf16 v[32:35], v[52:55], v[92:95], v[32:35]
	v_mfma_f32_16x16x32_bf16 v[36:39], v[48:51], v[96:99], 0
	v_mfma_f32_16x16x32_bf16 v[36:39], v[52:55], v[100:103], v[36:39]
	v_mfma_f32_16x16x32_bf16 v[40:43], v[48:51], v[104:107], 0
	v_mfma_f32_16x16x32_bf16 v[40:43], v[52:55], v[108:111], v[40:43]
	v_mfma_f32_16x16x32_bf16 v[44:47], v[48:51], v[112:115], 0
	v_mfma_f32_16x16x32_bf16 v[44:47], v[52:55], v[116:119], v[44:47]
	v_cvt_pk_bf16_f32 v16, v16, v17
	v_cvt_pk_bf16_f32 v17, v18, v19
	global_store_dwordx2 v4, v[16:17], s[0:1]
	v_cvt_pk_bf16_f32 v20, v20, v21
	v_cvt_pk_bf16_f32 v21, v22, v23
	global_store_dwordx2 v4, v[20:21], s[0:1] offset:512
	v_cvt_pk_bf16_f32 v24, v24, v25
	v_cvt_pk_bf16_f32 v25, v26, v27
	global_store_dwordx2 v5, v[24:25], s[0:1]
	v_cvt_pk_bf16_f32 v28, v28, v29
	v_cvt_pk_bf16_f32 v29, v30, v31
	global_store_dwordx2 v5, v[28:29], s[0:1] offset:512
	v_cvt_pk_bf16_f32 v32, v32, v33
	v_cvt_pk_bf16_f32 v33, v34, v35
	global_store_dwordx2 v6, v[32:33], s[0:1]
	v_cvt_pk_bf16_f32 v36, v36, v37
	v_cvt_pk_bf16_f32 v37, v38, v39
	global_store_dwordx2 v6, v[36:37], s[0:1] offset:512
	v_cvt_pk_bf16_f32 v40, v40, v41
	v_cvt_pk_bf16_f32 v41, v42, v43
	global_store_dwordx2 v11, v[40:41], s[0:1]
	s_nop 1
	v_cvt_pk_bf16_f32 v44, v44, v45
	v_cvt_pk_bf16_f32 v45, v46, v47
	global_store_dwordx2 v11, v[44:45], s[0:1] offset:512
	s_branch .LBB0_220
